# stack20 with the K/V LDS-DMA block (address SALU plus three DMAs) issued early in the step, right after the first QK MFMA's K reads
# speedup vs baseline: 1.0084x; 1.0045x over previous
; DI void finishSM(f32x16& p0, f32x16& p1, float alpha, float& l_reg, bf16x8& pa0, bf16x8& pa1, bf16x8& pa2, bf16x8& pa3) {
; #pragma unroll
;     for (int r = 0; r < 16; ++r) p1[r] = __builtin_amdgcn_exp2f(p1[r]);
;     float ps = 0;
; #pragma unroll
;     for (int r = 0; r < 16; ++r) ps += p0[r];
; #pragma unroll
;     for (int r = 0; r < 16; ++r) ps += p1[r];
;     { auto rr = __builtin_amdgcn_permlane32_swap(__float_as_uint(ps), __float_as_uint(ps), false, false); ps = __uint_as_float(rr[0]) + __uint_as_float(rr[1]); }
;     l_reg = l_reg * alpha + ps;
;     ...
;     AT_PK4(p0, 0, pa0); AT_PK4(p0, 8, pa1); AT_PK4(p1, 0, pa2); AT_PK4(p1, 8, pa3);
;     ...
; }
; DI void qkt(f32x16& p0, f32x16& p1, const char* Ks, const bf16x8* qr, const f32x16& negm, int r32, int hi) {
; #pragma unroll
;     for (int d0 = 0; d0 < 4; ++d0) { const int cb = (d0 * 16 + hi * 8) * 2;
;         const bf16x8 b0 = *reinterpret_cast<const bf16x8*>(Ks + AT_KSWZ(r32, cb));
;         const bf16x8 b1 = *reinterpret_cast<const bf16x8*>(Ks + AT_KSWZ(32 + r32, cb));
;         p0 = __builtin_amdgcn_mfma_f32_32x32x16_bf16(b0, qr[d0], d0 == 0 ? negm : p0, 0, 0, 0);
;         p1 = __builtin_amdgcn_mfma_f32_32x32x16_bf16(b1, qr[d0], d0 == 0 ? negm : p1, 0, 0, 0); }
; }
.LBB4_702:
	s_lshl_b32 s26, s66, 13
	s_add_i32 s26, s26, 0
	v_add_u32_e32 v72, s26, v205
	v_add_u32_e32 v112, s26, v206
	v_add_u32_e32 v180, s26, v207
	s_waitcnt lgkmcnt(1)
	v_mfma_f32_32x32x16_bf16 v[128:143], v[64:67], v[156:159], v[80:95]
	ds_read_b128 v[64:67], v72 offset:49152
	ds_read_b128 v[72:75], v72 offset:53248
	ds_read_b128 v[76:79], v112 offset:49152
	ds_read_b128 v[220:223], v112 offset:53248
	s_add_u32 s74, s46, s28
	s_addc_u32 s75, s47, s29
	s_add_u32 s78, s74, 0x23808000
	s_addc_u32 s79, s75, 0
	s_add_u32 s80, s74, 0x2380a000
	s_add_u32 s76, s46, s30
	s_addc_u32 s77, s47, s31
	s_add_u32 s82, s76, 0x21804000
	s_addc_u32 s83, s77, 0
	s_lshl_b32 s92, s64, 14
	s_add_i32 s92, s92, s94
	s_mov_b32 m0, s92
	s_lshl_b32 s96, s64, 13
	global_load_lds_dwordx4 v249, s[78:79]
	s_addk_i32 s92, 0x400
	s_mov_b32 m0, s92
	s_add_i32 s96, s96, s95
	global_load_lds_dwordx4 v250, s[78:79]
	s_nop 0
	s_mov_b32 m0, s96
	s_nop 0
	global_load_lds_dwordx4 v251, s[82:83]
	v_exp_f32_e32 v186, v97
	v_exp_f32_e32 v213, v98
	v_exp_f32_e32 v214, v99
	v_exp_f32_e32 v219, v100
	v_exp_f32_e32 v228, v101
	s_waitcnt lgkmcnt(4)
	v_mfma_f32_32x32x16_bf16 v[112:127], v[68:71], v[156:159], v[80:95]
	ds_read_b128 v[68:71], v180 offset:49152
	ds_read_b128 v[224:227], v180 offset:53248
	v_exp_f32_e32 v180, v96
	v_cvt_pk_bf16_f32 v96, v216, v218
	v_cvt_pk_bf16_f32 v97, v179, v217
	v_cvt_pk_bf16_f32 v98, v177, v215
	v_cvt_pk_bf16_f32 v99, v176, v178
	s_waitcnt lgkmcnt(4)
	v_mfma_f32_32x32x16_bf16 v[112:127], v[72:75], v[152:155], v[112:127]
	v_add_f32_e32 v75, 0, v216
	v_add_f32_e32 v75, v218, v75
	v_add_f32_e32 v75, v179, v75
	v_add_f32_e32 v75, v217, v75
	v_add_f32_e32 v75, v177, v75
	v_add_f32_e32 v75, v215, v75
	v_add_f32_e32 v75, v176, v75
	v_mfma_f32_32x32x16_bf16 v[128:143], v[64:67], v[152:155], v[128:143]
	v_add_f32_e32 v75, v178, v75
	v_add_f32_e32 v75, v173, v75
	v_add_f32_e32 v75, v175, v75
	v_add_f32_e32 v75, v171, v75
	v_add_f32_e32 v75, v174, v75
	v_add_f32_e32 v75, v169, v75
	v_add_f32_e32 v75, v172, v75
	s_waitcnt lgkmcnt(3)
	v_mfma_f32_32x32x16_bf16 v[128:143], v[76:79], v[148:151], v[128:143]
	v_add_f32_e32 v75, v168, v75
	v_add_f32_e32 v75, v170, v75
	v_add_f32_e32 v75, v180, v75
	v_add_f32_e32 v75, v186, v75
	v_exp_f32_e32 v64, v102
	v_exp_f32_e32 v65, v103
	v_exp_f32_e32 v66, v104
	s_waitcnt lgkmcnt(2)
	v_mfma_f32_32x32x16_bf16 v[112:127], v[220:223], v[148:151], v[112:127]
	v_exp_f32_e32 v67, v105
	v_exp_f32_e32 v105, v106
	v_exp_f32_e32 v106, v107
	v_exp_f32_e32 v107, v108
	v_exp_f32_e32 v72, v109
	v_exp_f32_e32 v73, v110
	v_exp_f32_e32 v74, v111
	s_waitcnt lgkmcnt(1)
	v_mfma_f32_32x32x16_bf16 v[128:143], v[68:71], v[144:147], v[128:143]
	v_add_f32_e32 v68, v213, v75
	v_add_f32_e32 v68, v214, v68
	v_add_f32_e32 v68, v219, v68
	v_add_f32_e32 v68, v228, v68
	v_add_f32_e32 v68, v64, v68
	v_add_f32_e32 v68, v65, v68
	v_add_f32_e32 v68, v66, v68
	v_add_f32_e32 v68, v67, v68
	s_waitcnt lgkmcnt(0)
	v_mfma_f32_32x32x16_bf16 v[112:127], v[224:227], v[144:147], v[112:127]
	v_add_f32_e32 v68, v105, v68
	v_add_f32_e32 v68, v106, v68
	v_add_f32_e32 v68, v107, v68
	v_add_f32_e32 v68, v72, v68
	v_add_f32_e32 v68, v73, v68
	v_add_f32_e32 v183, v74, v68
	v_cvt_pk_bf16_f32 v108, v173, v175
	v_cvt_pk_bf16_f32 v109, v171, v174
	v_cvt_pk_bf16_f32 v110, v169, v172
	v_cvt_pk_bf16_f32 v111, v168, v170
	v_cvt_pk_bf16_f32 v100, v180, v186
	v_cvt_pk_bf16_f32 v101, v213, v214
	v_cvt_pk_bf16_f32 v102, v219, v228
	v_cvt_pk_bf16_f32 v103, v64, v65
	v_cvt_pk_bf16_f32 v104, v66, v67
	v_cvt_pk_bf16_f32 v105, v105, v106
	v_cvt_pk_bf16_f32 v106, v107, v72
	v_cvt_pk_bf16_f32 v107, v73, v74
	s_addc_u32 s81, s75, 0
	s_andn2_b64 vcc, exec, s[2:3]
	s_cbranch_vccnz .LBB4_704
	s_mov_b64 s[2:3], s[8:9]
	global_store_dwordx2 v189, v[184:185], s[2:3] nt

; DI void finishSM(f32x16& p0, f32x16& p1, float alpha, float& l_reg, bf16x8& pa0, bf16x8& pa1, bf16x8& pa2, bf16x8& pa3) {
; #pragma unroll
;     for (int r = 0; r < 16; ++r) p1[r] = __builtin_amdgcn_exp2f(p1[r]);
;     float ps = 0;
; #pragma unroll
;     for (int r = 0; r < 16; ++r) ps += p0[r];
; #pragma unroll
;     for (int r = 0; r < 16; ++r) ps += p1[r];
;     { auto rr = __builtin_amdgcn_permlane32_swap(__float_as_uint(ps), __float_as_uint(ps), false, false); ps = __uint_as_float(rr[0]) + __uint_as_float(rr[1]); }
;     l_reg = l_reg * alpha + ps;
;     ...
;     AT_PK4(p0, 0, pa0); AT_PK4(p0, 8, pa1); AT_PK4(p1, 0, pa2); AT_PK4(p1, 8, pa3);
;     ...
; }
; DI void qkt(f32x16& p0, f32x16& p1, const char* Ks, const bf16x8* qr, const f32x16& negm, int r32, int hi) {
; #pragma unroll
;     for (int d0 = 0; d0 < 4; ++d0) { const int cb = (d0 * 16 + hi * 8) * 2;
;         const bf16x8 b0 = *reinterpret_cast<const bf16x8*>(Ks + AT_KSWZ(r32, cb));
;         const bf16x8 b1 = *reinterpret_cast<const bf16x8*>(Ks + AT_KSWZ(32 + r32, cb));
;         p0 = __builtin_amdgcn_mfma_f32_32x32x16_bf16(b0, qr[d0], d0 == 0 ? negm : p0, 0, 0, 0);
;         p1 = __builtin_amdgcn_mfma_f32_32x32x16_bf16(b1, qr[d0], d0 == 0 ? negm : p1, 0, 0, 0); }
; }
.LBB4_723:
	v_exp_f32_e32 v186, v128
	v_exp_f32_e32 v230, v129
	v_exp_f32_e32 v231, v130
	v_exp_f32_e32 v232, v131
	v_exp_f32_e32 v233, v132
	v_exp_f32_e32 v234, v133
	v_exp_f32_e32 v235, v134
	v_exp_f32_e32 v236, v135
	v_exp_f32_e32 v237, v136
	v_exp_f32_e32 v238, v137
	v_exp_f32_e32 v239, v138
	v_exp_f32_e32 v240, v139
	v_exp_f32_e32 v241, v140
	v_exp_f32_e32 v242, v141
	v_exp_f32_e32 v243, v142
	v_exp_f32_e32 v244, v143
	v_add_u32_e32 v101, s78, v205
	v_add_u32_e32 v102, s78, v206
	v_add_u32_e32 v103, s78, v207
	ds_read_b128 v[172:175], v101 offset:49152
	ds_read_b128 v[176:179], v101 offset:53248
	ds_read_b128 v[214:217], v102 offset:49152
	ds_read_b128 v[218:221], v102 offset:53248
	ds_read_b128 v[222:225], v103 offset:49152
	ds_read_b128 v[226:229], v103 offset:53248
	v_exp_f32_e32 v112, v112
	v_exp_f32_e32 v113, v113
	v_exp_f32_e32 v114, v114
	s_waitcnt lgkmcnt(7)
	v_mfma_f32_32x32x16_bf16 v[128:143], v[96:99], v[156:159], v[80:95]
	s_add_u32 s78, s74, 0x2380c000
	s_addc_u32 s79, s75, 0
	s_add_u32 s74, s74, 0x2380e000
	s_addc_u32 s75, s75, 0
	s_add_u32 s76, s76, 0x21806000
	s_addc_u32 s77, s77, 0
	s_lshl_b32 s92, s65, 14
	s_add_i32 s92, s92, s94
	s_mov_b32 m0, s92
	s_lshl_b32 s96, s65, 13
	global_load_lds_dwordx4 v249, s[78:79]
	s_addk_i32 s92, 0x400
	s_mov_b32 m0, s92
	s_add_i32 s96, s96, s95
	global_load_lds_dwordx4 v250, s[78:79]
	s_nop 0
	s_mov_b32 m0, s96
	s_nop 0
	global_load_lds_dwordx4 v251, s[76:77]
	s_nop 0
	v_exp_f32_e32 v115, v115
	v_exp_f32_e32 v116, v116
	v_exp_f32_e32 v117, v117
	v_exp_f32_e32 v118, v118
	v_exp_f32_e32 v119, v119
	s_waitcnt lgkmcnt(6)
	v_mfma_f32_32x32x16_bf16 v[96:111], v[168:171], v[156:159], v[80:95]
	v_exp_f32_e32 v168, v120
	v_add_f32_e32 v120, 0, v186
	v_add_f32_e32 v120, v230, v120
	v_add_f32_e32 v120, v231, v120
	v_add_f32_e32 v120, v232, v120
	v_add_f32_e32 v120, v233, v120
	v_add_f32_e32 v120, v234, v120
	v_add_f32_e32 v120, v235, v120
	v_add_f32_e32 v120, v236, v120
	v_add_f32_e32 v120, v237, v120
	v_add_f32_e32 v120, v238, v120
	s_waitcnt lgkmcnt(5)
	v_mfma_f32_32x32x16_bf16 v[128:143], v[172:175], v[152:155], v[128:143]
	v_add_f32_e32 v120, v239, v120
	v_add_f32_e32 v120, v240, v120
	v_add_f32_e32 v120, v241, v120
	v_add_f32_e32 v120, v242, v120
	v_add_f32_e32 v120, v243, v120
	v_add_f32_e32 v120, v244, v120
	v_add_f32_e32 v120, v112, v120
	s_waitcnt lgkmcnt(4)
	v_mfma_f32_32x32x16_bf16 v[96:111], v[176:179], v[152:155], v[96:111]
	v_add_f32_e32 v120, v113, v120
	v_add_f32_e32 v120, v114, v120
	v_add_f32_e32 v120, v115, v120
	v_add_f32_e32 v120, v116, v120
	v_exp_f32_e32 v169, v121
	v_add_f32_e32 v120, v117, v120
	v_exp_f32_e32 v170, v122
	s_waitcnt lgkmcnt(3)
	v_mfma_f32_32x32x16_bf16 v[128:143], v[214:217], v[148:151], v[128:143]
	v_add_f32_e32 v120, v118, v120
	v_exp_f32_e32 v171, v123
	v_add_f32_e32 v120, v119, v120
	v_exp_f32_e32 v172, v124
	v_add_f32_e32 v120, v168, v120
	v_exp_f32_e32 v173, v125
	v_add_f32_e32 v120, v169, v120
	s_waitcnt lgkmcnt(2)
	v_mfma_f32_32x32x16_bf16 v[96:111], v[218:221], v[148:151], v[96:111]
	v_exp_f32_e32 v174, v126
	v_add_f32_e32 v120, v170, v120
	v_exp_f32_e32 v175, v127
	v_add_f32_e32 v120, v171, v120
	v_add_f32_e32 v120, v172, v120
	v_add_f32_e32 v120, v173, v120
	v_add_f32_e32 v120, v174, v120
	s_waitcnt lgkmcnt(1)
	v_mfma_f32_32x32x16_bf16 v[128:143], v[222:225], v[144:147], v[128:143]
	v_add_f32_e32 v213, v175, v120
	v_cvt_pk_bf16_f32 v120, v186, v230
	v_cvt_pk_bf16_f32 v121, v231, v232
	v_cvt_pk_bf16_f32 v122, v233, v234
	v_cvt_pk_bf16_f32 v123, v235, v236
	v_cvt_pk_bf16_f32 v124, v237, v238
	s_waitcnt lgkmcnt(0)
	v_mfma_f32_32x32x16_bf16 v[96:111], v[226:229], v[144:147], v[96:111]
	v_cvt_pk_bf16_f32 v125, v239, v240
	v_cvt_pk_bf16_f32 v126, v241, v242
	v_cvt_pk_bf16_f32 v127, v243, v244
	v_cvt_pk_bf16_f32 v112, v112, v113
	v_cvt_pk_bf16_f32 v113, v114, v115
	v_cvt_pk_bf16_f32 v114, v116, v117
	v_cvt_pk_bf16_f32 v115, v118, v119
	v_cvt_pk_bf16_f32 v116, v168, v169
	v_cvt_pk_bf16_f32 v117, v170, v171
	v_cvt_pk_bf16_f32 v118, v172, v173
	v_cvt_pk_bf16_f32 v119, v174, v175
	s_and_b64 vcc, exec, s[2:3]
	s_cbranch_vccnz .LBB4_725
	s_mov_b64 s[2:3], s[8:9]
	global_store_dwordx2 v189, v[184:185], s[2:3] nt

; DI void finishSM(f32x16& p0, f32x16& p1, float alpha, float& l_reg, bf16x8& pa0, bf16x8& pa1, bf16x8& pa2, bf16x8& pa3) {
; #pragma unroll
;     for (int r = 0; r < 16; ++r) p1[r] = __builtin_amdgcn_exp2f(p1[r]);
;     float ps = 0;
; #pragma unroll
;     for (int r = 0; r < 16; ++r) ps += p0[r];
; #pragma unroll
;     for (int r = 0; r < 16; ++r) ps += p1[r];
;     { auto rr = __builtin_amdgcn_permlane32_swap(__float_as_uint(ps), __float_as_uint(ps), false, false); ps = __uint_as_float(rr[0]) + __uint_as_float(rr[1]); }
;     l_reg = l_reg * alpha + ps;
;     ...
;     AT_PK4(p0, 0, pa0); AT_PK4(p0, 8, pa1); AT_PK4(p1, 0, pa2); AT_PK4(p1, 8, pa3);
;     ...
; }
; DI void qkt(f32x16& p0, f32x16& p1, const char* Ks, const bf16x8* qr, const f32x16& negm, int r32, int hi) {
; #pragma unroll
;     for (int d0 = 0; d0 < 4; ++d0) { const int cb = (d0 * 16 + hi * 8) * 2;
;         const bf16x8 b0 = *reinterpret_cast<const bf16x8*>(Ks + AT_KSWZ(r32, cb));
;         const bf16x8 b1 = *reinterpret_cast<const bf16x8*>(Ks + AT_KSWZ(32 + r32, cb));
;         p0 = __builtin_amdgcn_mfma_f32_32x32x16_bf16(b0, qr[d0], d0 == 0 ? negm : p0, 0, 0, 0);
;         p1 = __builtin_amdgcn_mfma_f32_32x32x16_bf16(b1, qr[d0], d0 == 0 ? negm : p1, 0, 0, 0); }
; }
.LBB4_775:
	s_lshl_b32 s20, s30, 13
	s_add_i32 s20, s20, 0
	v_add_u32_e32 v72, s20, v208
	v_add_u32_e32 v112, s20, v209
	v_add_u32_e32 v180, s20, v210
	s_waitcnt lgkmcnt(1)
	v_mfma_f32_32x32x16_bf16 v[128:143], v[64:67], v[156:159], v[80:95]
	ds_read_b128 v[64:67], v72 offset:49152
	ds_read_b128 v[72:75], v72 offset:53248
	ds_read_b128 v[76:79], v112 offset:49152
	ds_read_b128 v[224:227], v112 offset:53248
	s_add_u32 s34, s46, s16
	s_addc_u32 s35, s47, s17
	s_add_u32 s24, s34, 0x23808000
	s_addc_u32 s25, s35, 0
	s_add_u32 s66, s34, 0x2380a000
	s_add_u32 s37, s46, s18
	s_addc_u32 s64, s47, s19
	s_add_u32 s74, s37, 0x21884000
	s_addc_u32 s75, s64, 0
	s_lshl_b32 s92, s15, 14
	s_add_i32 s92, s92, s94
	s_mov_b32 m0, s92
	s_lshl_b32 s96, s15, 13
	global_load_lds_dwordx4 v249, s[24:25]
	s_addk_i32 s92, 0x400
	s_mov_b32 m0, s92
	s_add_i32 s96, s96, s95
	global_load_lds_dwordx4 v250, s[24:25]
	s_nop 0
	s_mov_b32 m0, s96
	s_nop 0
	global_load_lds_dwordx4 v251, s[74:75]
	v_exp_f32_e32 v182, v97
	v_exp_f32_e32 v217, v98
	v_exp_f32_e32 v218, v99
	v_exp_f32_e32 v223, v100
	v_exp_f32_e32 v232, v101
	s_waitcnt lgkmcnt(4)
	v_mfma_f32_32x32x16_bf16 v[112:127], v[68:71], v[156:159], v[80:95]
	ds_read_b128 v[68:71], v180 offset:49152
	ds_read_b128 v[228:231], v180 offset:53248
	v_exp_f32_e32 v180, v96
	v_cvt_pk_bf16_f32 v96, v220, v222
	v_cvt_pk_bf16_f32 v97, v179, v221
	v_cvt_pk_bf16_f32 v98, v177, v219
	v_cvt_pk_bf16_f32 v99, v176, v178
	s_waitcnt lgkmcnt(4)
	v_mfma_f32_32x32x16_bf16 v[112:127], v[72:75], v[152:155], v[112:127]
	v_add_f32_e32 v75, 0, v220
	v_add_f32_e32 v75, v222, v75
	v_add_f32_e32 v75, v179, v75
	v_add_f32_e32 v75, v221, v75
	v_add_f32_e32 v75, v177, v75
	v_add_f32_e32 v75, v219, v75
	v_add_f32_e32 v75, v176, v75
	v_mfma_f32_32x32x16_bf16 v[128:143], v[64:67], v[152:155], v[128:143]
	v_add_f32_e32 v75, v178, v75
	v_add_f32_e32 v75, v173, v75
	v_add_f32_e32 v75, v175, v75
	v_add_f32_e32 v75, v171, v75
	v_add_f32_e32 v75, v174, v75
	v_add_f32_e32 v75, v169, v75
	v_add_f32_e32 v75, v172, v75
	s_waitcnt lgkmcnt(3)
	v_mfma_f32_32x32x16_bf16 v[128:143], v[76:79], v[148:151], v[128:143]
	v_add_f32_e32 v75, v168, v75
	v_add_f32_e32 v75, v170, v75
	v_add_f32_e32 v75, v180, v75
	v_add_f32_e32 v75, v182, v75
	v_exp_f32_e32 v64, v102
	v_exp_f32_e32 v65, v103
	v_exp_f32_e32 v66, v104
	s_waitcnt lgkmcnt(2)
	v_mfma_f32_32x32x16_bf16 v[112:127], v[224:227], v[148:151], v[112:127]
	v_exp_f32_e32 v67, v105
	v_exp_f32_e32 v105, v106
	v_exp_f32_e32 v106, v107
	v_exp_f32_e32 v107, v108
	v_exp_f32_e32 v72, v109
	v_exp_f32_e32 v73, v110
	v_exp_f32_e32 v74, v111
	s_waitcnt lgkmcnt(1)
	v_mfma_f32_32x32x16_bf16 v[128:143], v[68:71], v[144:147], v[128:143]
	v_add_f32_e32 v68, v217, v75
	v_add_f32_e32 v68, v218, v68
	v_add_f32_e32 v68, v223, v68
	v_add_f32_e32 v68, v232, v68
	v_add_f32_e32 v68, v64, v68
	v_add_f32_e32 v68, v65, v68
	v_add_f32_e32 v68, v66, v68
	v_add_f32_e32 v68, v67, v68
	s_waitcnt lgkmcnt(0)
	v_mfma_f32_32x32x16_bf16 v[112:127], v[228:231], v[144:147], v[112:127]
	v_add_f32_e32 v68, v105, v68
	v_add_f32_e32 v68, v106, v68
	v_add_f32_e32 v68, v107, v68
	v_add_f32_e32 v68, v72, v68
	v_add_f32_e32 v68, v73, v68
	v_add_f32_e32 v215, v74, v68
	v_cvt_pk_bf16_f32 v108, v173, v175
	v_cvt_pk_bf16_f32 v109, v171, v174
	v_cvt_pk_bf16_f32 v110, v169, v172
	v_cvt_pk_bf16_f32 v111, v168, v170
	v_cvt_pk_bf16_f32 v100, v180, v182
	v_cvt_pk_bf16_f32 v101, v217, v218
	v_cvt_pk_bf16_f32 v102, v223, v232
	v_cvt_pk_bf16_f32 v103, v64, v65
	v_cvt_pk_bf16_f32 v104, v66, v67
	v_cvt_pk_bf16_f32 v105, v105, v106
	v_cvt_pk_bf16_f32 v106, v107, v72
	v_cvt_pk_bf16_f32 v107, v73, v74
	s_addc_u32 s67, s35, 0
	s_andn2_b64 vcc, exec, s[2:3]
	s_cbranch_vccnz .LBB4_777
	s_mov_b64 s[2:3], s[8:9]
	global_store_dwordx2 v193, v[184:185], s[2:3] nt

; DI void finishSM(f32x16& p0, f32x16& p1, float alpha, float& l_reg, bf16x8& pa0, bf16x8& pa1, bf16x8& pa2, bf16x8& pa3) {
; #pragma unroll
;     for (int r = 0; r < 16; ++r) p1[r] = __builtin_amdgcn_exp2f(p1[r]);
;     float ps = 0;
; #pragma unroll
;     for (int r = 0; r < 16; ++r) ps += p0[r];
; #pragma unroll
;     for (int r = 0; r < 16; ++r) ps += p1[r];
;     { auto rr = __builtin_amdgcn_permlane32_swap(__float_as_uint(ps), __float_as_uint(ps), false, false); ps = __uint_as_float(rr[0]) + __uint_as_float(rr[1]); }
;     l_reg = l_reg * alpha + ps;
;     ...
;     AT_PK4(p0, 0, pa0); AT_PK4(p0, 8, pa1); AT_PK4(p1, 0, pa2); AT_PK4(p1, 8, pa3);
;     ...
; }
; DI void qkt(f32x16& p0, f32x16& p1, const char* Ks, const bf16x8* qr, const f32x16& negm, int r32, int hi) {
; #pragma unroll
;     for (int d0 = 0; d0 < 4; ++d0) { const int cb = (d0 * 16 + hi * 8) * 2;
;         const bf16x8 b0 = *reinterpret_cast<const bf16x8*>(Ks + AT_KSWZ(r32, cb));
;         const bf16x8 b1 = *reinterpret_cast<const bf16x8*>(Ks + AT_KSWZ(32 + r32, cb));
;         p0 = __builtin_amdgcn_mfma_f32_32x32x16_bf16(b0, qr[d0], d0 == 0 ? negm : p0, 0, 0, 0);
;         p1 = __builtin_amdgcn_mfma_f32_32x32x16_bf16(b1, qr[d0], d0 == 0 ? negm : p1, 0, 0, 0); }
; }
.LBB4_796:
	v_exp_f32_e32 v182, v128
	v_exp_f32_e32 v234, v129
	v_exp_f32_e32 v235, v130
	v_exp_f32_e32 v236, v131
	v_exp_f32_e32 v237, v132
	v_exp_f32_e32 v238, v133
	v_exp_f32_e32 v239, v134
	v_exp_f32_e32 v240, v135
	v_exp_f32_e32 v241, v136
	v_exp_f32_e32 v242, v137
	v_exp_f32_e32 v243, v138
	v_exp_f32_e32 v244, v139
	v_exp_f32_e32 v245, v140
	v_exp_f32_e32 v246, v141
	v_exp_f32_e32 v247, v142
	v_exp_f32_e32 v248, v143
	v_add_u32_e32 v101, s65, v208
	v_add_u32_e32 v102, s65, v209
	v_add_u32_e32 v103, s65, v210
	ds_read_b128 v[172:175], v101 offset:49152
	ds_read_b128 v[176:179], v101 offset:53248
	ds_read_b128 v[218:221], v102 offset:49152
	ds_read_b128 v[222:225], v102 offset:53248
	ds_read_b128 v[226:229], v103 offset:49152
	ds_read_b128 v[230:233], v103 offset:53248
	v_exp_f32_e32 v112, v112
	v_exp_f32_e32 v113, v113
	v_exp_f32_e32 v114, v114
	s_waitcnt lgkmcnt(7)
	v_mfma_f32_32x32x16_bf16 v[128:143], v[96:99], v[156:159], v[80:95]
	s_add_u32 s24, s34, 0x2380c000
	s_addc_u32 s25, s35, 0
	s_add_u32 s34, s34, 0x2380e000
	s_addc_u32 s35, s35, 0
	s_add_u32 s66, s37, 0x21886000
	s_addc_u32 s67, s64, 0
	s_lshl_b32 s92, s29, 14
	s_add_i32 s92, s92, s94
	s_mov_b32 m0, s92
	s_lshl_b32 s96, s29, 13
	global_load_lds_dwordx4 v249, s[24:25]
	s_addk_i32 s92, 0x400
	s_mov_b32 m0, s92
	s_add_i32 s96, s96, s95
	global_load_lds_dwordx4 v250, s[24:25]
	s_nop 0
	s_mov_b32 m0, s96
	s_nop 0
	global_load_lds_dwordx4 v251, s[66:67]
	s_nop 0
	v_exp_f32_e32 v115, v115
	v_exp_f32_e32 v116, v116
	v_exp_f32_e32 v117, v117
	v_exp_f32_e32 v118, v118
	v_exp_f32_e32 v119, v119
	s_waitcnt lgkmcnt(6)
	v_mfma_f32_32x32x16_bf16 v[96:111], v[168:171], v[156:159], v[80:95]
	v_exp_f32_e32 v168, v120
	v_add_f32_e32 v120, 0, v182
	v_add_f32_e32 v120, v234, v120
	v_add_f32_e32 v120, v235, v120
	v_add_f32_e32 v120, v236, v120
	v_add_f32_e32 v120, v237, v120
	v_add_f32_e32 v120, v238, v120
	v_add_f32_e32 v120, v239, v120
	v_add_f32_e32 v120, v240, v120
	v_add_f32_e32 v120, v241, v120
	v_add_f32_e32 v120, v242, v120
	s_waitcnt lgkmcnt(5)
	v_mfma_f32_32x32x16_bf16 v[128:143], v[172:175], v[152:155], v[128:143]
	v_add_f32_e32 v120, v243, v120
	v_add_f32_e32 v120, v244, v120
	v_add_f32_e32 v120, v245, v120
	v_add_f32_e32 v120, v246, v120
	v_add_f32_e32 v120, v247, v120
	v_add_f32_e32 v120, v248, v120
	v_add_f32_e32 v120, v112, v120
	s_waitcnt lgkmcnt(4)
	v_mfma_f32_32x32x16_bf16 v[96:111], v[176:179], v[152:155], v[96:111]
	v_add_f32_e32 v120, v113, v120
	v_add_f32_e32 v120, v114, v120
	v_add_f32_e32 v120, v115, v120
	v_add_f32_e32 v120, v116, v120
	v_exp_f32_e32 v169, v121
	v_add_f32_e32 v120, v117, v120
	v_exp_f32_e32 v170, v122
	s_waitcnt lgkmcnt(3)
	v_mfma_f32_32x32x16_bf16 v[128:143], v[218:221], v[148:151], v[128:143]
	v_add_f32_e32 v120, v118, v120
	v_exp_f32_e32 v171, v123
	v_add_f32_e32 v120, v119, v120
	v_exp_f32_e32 v172, v124
	v_add_f32_e32 v120, v168, v120
	v_exp_f32_e32 v173, v125
	v_add_f32_e32 v120, v169, v120
	s_waitcnt lgkmcnt(2)
	v_mfma_f32_32x32x16_bf16 v[96:111], v[222:225], v[148:151], v[96:111]
	v_exp_f32_e32 v174, v126
	v_add_f32_e32 v120, v170, v120
	v_exp_f32_e32 v175, v127
	v_add_f32_e32 v120, v171, v120
	v_add_f32_e32 v120, v172, v120
	v_add_f32_e32 v120, v173, v120
	v_add_f32_e32 v120, v174, v120
	s_waitcnt lgkmcnt(1)
	v_mfma_f32_32x32x16_bf16 v[128:143], v[226:229], v[144:147], v[128:143]
	v_add_f32_e32 v217, v175, v120
	v_cvt_pk_bf16_f32 v120, v182, v234
	v_cvt_pk_bf16_f32 v121, v235, v236
	v_cvt_pk_bf16_f32 v122, v237, v238
	v_cvt_pk_bf16_f32 v123, v239, v240
	v_cvt_pk_bf16_f32 v124, v241, v242
	s_waitcnt lgkmcnt(0)
	v_mfma_f32_32x32x16_bf16 v[96:111], v[230:233], v[144:147], v[96:111]
	v_cvt_pk_bf16_f32 v125, v243, v244
	v_cvt_pk_bf16_f32 v126, v245, v246
	v_cvt_pk_bf16_f32 v127, v247, v248
	v_cvt_pk_bf16_f32 v112, v112, v113
	v_cvt_pk_bf16_f32 v113, v114, v115
	v_cvt_pk_bf16_f32 v114, v116, v117
	v_cvt_pk_bf16_f32 v115, v118, v119
	v_cvt_pk_bf16_f32 v116, v168, v169
	v_cvt_pk_bf16_f32 v117, v170, v171
	v_cvt_pk_bf16_f32 v118, v172, v173
	v_cvt_pk_bf16_f32 v119, v174, v175
	s_and_b64 vcc, exec, s[2:3]
	s_cbranch_vccnz .LBB4_798
	s_mov_b64 s[2:3], s[8:9]
	global_store_dwordx2 v193, v[184:185], s[2:3] nt

; DI void finishSM(f32x16& p0, f32x16& p1, float alpha, float& l_reg, bf16x8& pa0, bf16x8& pa1, bf16x8& pa2, bf16x8& pa3) {
; #pragma unroll
;     for (int r = 0; r < 16; ++r) p1[r] = __builtin_amdgcn_exp2f(p1[r]);
;     float ps = 0;
; #pragma unroll
;     for (int r = 0; r < 16; ++r) ps += p0[r];
; #pragma unroll
;     for (int r = 0; r < 16; ++r) ps += p1[r];
;     { auto rr = __builtin_amdgcn_permlane32_swap(__float_as_uint(ps), __float_as_uint(ps), false, false); ps = __uint_as_float(rr[0]) + __uint_as_float(rr[1]); }
;     l_reg = l_reg * alpha + ps;
;     ...
;     AT_PK4(p0, 0, pa0); AT_PK4(p0, 8, pa1); AT_PK4(p1, 0, pa2); AT_PK4(p1, 8, pa3);
;     ...
; }
; DI void qkt(f32x16& p0, f32x16& p1, const char* Ks, const bf16x8* qr, const f32x16& negm, int r32, int hi) {
; #pragma unroll
;     for (int d0 = 0; d0 < 4; ++d0) { const int cb = (d0 * 16 + hi * 8) * 2;
;         const bf16x8 b0 = *reinterpret_cast<const bf16x8*>(Ks + AT_KSWZ(r32, cb));
;         const bf16x8 b1 = *reinterpret_cast<const bf16x8*>(Ks + AT_KSWZ(32 + r32, cb));
;         p0 = __builtin_amdgcn_mfma_f32_32x32x16_bf16(b0, qr[d0], d0 == 0 ? negm : p0, 0, 0, 0);
;         p1 = __builtin_amdgcn_mfma_f32_32x32x16_bf16(b1, qr[d0], d0 == 0 ? negm : p1, 0, 0, 0); }
; }
.LBB4_849:
	s_lshl_b32 s26, s64, 13
	s_add_i32 s26, s26, 0
	v_add_u32_e32 v72, s26, v204
	v_add_u32_e32 v112, s26, v205
	v_add_u32_e32 v180, s26, v206
	s_waitcnt lgkmcnt(1)
	v_mfma_f32_32x32x16_bf16 v[128:143], v[64:67], v[156:159], v[80:95]
	ds_read_b128 v[64:67], v72 offset:49152
	ds_read_b128 v[72:75], v72 offset:53248
	ds_read_b128 v[76:79], v112 offset:49152
	ds_read_b128 v[220:223], v112 offset:53248
	s_add_u32 s66, s46, s28
	s_addc_u32 s67, s47, s29
	s_add_u32 s34, s66, 0x23808000
	s_addc_u32 s35, s67, 0
	s_add_u32 s76, s66, 0x2380a000
	s_add_u32 s74, s46, s24
	s_addc_u32 s75, s47, s25
	s_add_u32 s78, s74, 0x21804000
	s_addc_u32 s79, s75, 0
	s_lshl_b32 s92, s57, 14
	s_add_i32 s92, s92, s94
	s_mov_b32 m0, s92
	s_lshl_b32 s96, s57, 13
	global_load_lds_dwordx4 v249, s[34:35]
	s_addk_i32 s92, 0x400
	s_mov_b32 m0, s92
	s_add_i32 s96, s96, s95
	global_load_lds_dwordx4 v250, s[34:35]
	s_nop 0
	s_mov_b32 m0, s96
	s_nop 0
	global_load_lds_dwordx4 v251, s[78:79]
	v_exp_f32_e32 v182, v97
	v_exp_f32_e32 v213, v98
	v_exp_f32_e32 v214, v99
	v_exp_f32_e32 v219, v100
	v_exp_f32_e32 v228, v101
	s_waitcnt lgkmcnt(4)
	v_mfma_f32_32x32x16_bf16 v[112:127], v[68:71], v[156:159], v[80:95]
	ds_read_b128 v[68:71], v180 offset:49152
	ds_read_b128 v[224:227], v180 offset:53248
	v_exp_f32_e32 v180, v96
	v_cvt_pk_bf16_f32 v96, v216, v218
	v_cvt_pk_bf16_f32 v97, v179, v217
	v_cvt_pk_bf16_f32 v98, v177, v215
	v_cvt_pk_bf16_f32 v99, v176, v178
	s_waitcnt lgkmcnt(4)
	v_mfma_f32_32x32x16_bf16 v[112:127], v[72:75], v[152:155], v[112:127]
	v_add_f32_e32 v75, 0, v216
	v_add_f32_e32 v75, v218, v75
	v_add_f32_e32 v75, v179, v75
	v_add_f32_e32 v75, v217, v75
	v_add_f32_e32 v75, v177, v75
	v_add_f32_e32 v75, v215, v75
	v_add_f32_e32 v75, v176, v75
	v_mfma_f32_32x32x16_bf16 v[128:143], v[64:67], v[152:155], v[128:143]
	v_add_f32_e32 v75, v178, v75
	v_add_f32_e32 v75, v173, v75
	v_add_f32_e32 v75, v175, v75
	v_add_f32_e32 v75, v171, v75
	v_add_f32_e32 v75, v174, v75
	v_add_f32_e32 v75, v169, v75
	v_add_f32_e32 v75, v172, v75
	s_waitcnt lgkmcnt(3)
	v_mfma_f32_32x32x16_bf16 v[128:143], v[76:79], v[148:151], v[128:143]
	v_add_f32_e32 v75, v168, v75
	v_add_f32_e32 v75, v170, v75
	v_add_f32_e32 v75, v180, v75
	v_add_f32_e32 v75, v182, v75
	v_exp_f32_e32 v64, v102
	v_exp_f32_e32 v65, v103
	v_exp_f32_e32 v66, v104
	s_waitcnt lgkmcnt(2)
	v_mfma_f32_32x32x16_bf16 v[112:127], v[220:223], v[148:151], v[112:127]
	v_exp_f32_e32 v67, v105
	v_exp_f32_e32 v105, v106
	v_exp_f32_e32 v106, v107
	v_exp_f32_e32 v107, v108
	v_exp_f32_e32 v72, v109
	v_exp_f32_e32 v73, v110
	v_exp_f32_e32 v74, v111
	s_waitcnt lgkmcnt(1)
	v_mfma_f32_32x32x16_bf16 v[128:143], v[68:71], v[144:147], v[128:143]
	v_add_f32_e32 v68, v213, v75
	v_add_f32_e32 v68, v214, v68
	v_add_f32_e32 v68, v219, v68
	v_add_f32_e32 v68, v228, v68
	v_add_f32_e32 v68, v64, v68
	v_add_f32_e32 v68, v65, v68
	v_add_f32_e32 v68, v66, v68
	v_add_f32_e32 v68, v67, v68
	s_waitcnt lgkmcnt(0)
	v_mfma_f32_32x32x16_bf16 v[112:127], v[224:227], v[144:147], v[112:127]
	v_add_f32_e32 v68, v105, v68
	v_add_f32_e32 v68, v106, v68
	v_add_f32_e32 v68, v107, v68
	v_add_f32_e32 v68, v72, v68
	v_add_f32_e32 v68, v73, v68
	v_add_f32_e32 v211, v74, v68
	v_cvt_pk_bf16_f32 v108, v173, v175
	v_cvt_pk_bf16_f32 v109, v171, v174
	v_cvt_pk_bf16_f32 v110, v169, v172
	v_cvt_pk_bf16_f32 v111, v168, v170
	v_cvt_pk_bf16_f32 v100, v180, v182
	v_cvt_pk_bf16_f32 v101, v213, v214
	v_cvt_pk_bf16_f32 v102, v219, v228
	v_cvt_pk_bf16_f32 v103, v64, v65
	v_cvt_pk_bf16_f32 v104, v66, v67
	v_cvt_pk_bf16_f32 v105, v105, v106
	v_cvt_pk_bf16_f32 v106, v107, v72
	v_cvt_pk_bf16_f32 v107, v73, v74
	s_addc_u32 s77, s67, 0
	s_andn2_b64 vcc, exec, s[2:3]
	s_cbranch_vccnz .LBB4_851
	s_mov_b64 s[2:3], s[8:9]
	global_store_dwordx2 v188, v[184:185], s[2:3] nt

; DI void finishSM(f32x16& p0, f32x16& p1, float alpha, float& l_reg, bf16x8& pa0, bf16x8& pa1, bf16x8& pa2, bf16x8& pa3) {
; #pragma unroll
;     for (int r = 0; r < 16; ++r) p1[r] = __builtin_amdgcn_exp2f(p1[r]);
;     float ps = 0;
; #pragma unroll
;     for (int r = 0; r < 16; ++r) ps += p0[r];
; #pragma unroll
;     for (int r = 0; r < 16; ++r) ps += p1[r];
;     { auto rr = __builtin_amdgcn_permlane32_swap(__float_as_uint(ps), __float_as_uint(ps), false, false); ps = __uint_as_float(rr[0]) + __uint_as_float(rr[1]); }
;     l_reg = l_reg * alpha + ps;
;     ...
;     AT_PK4(p0, 0, pa0); AT_PK4(p0, 8, pa1); AT_PK4(p1, 0, pa2); AT_PK4(p1, 8, pa3);
;     ...
; }
; DI void qkt(f32x16& p0, f32x16& p1, const char* Ks, const bf16x8* qr, const f32x16& negm, int r32, int hi) {
; #pragma unroll
;     for (int d0 = 0; d0 < 4; ++d0) { const int cb = (d0 * 16 + hi * 8) * 2;
;         const bf16x8 b0 = *reinterpret_cast<const bf16x8*>(Ks + AT_KSWZ(r32, cb));
;         const bf16x8 b1 = *reinterpret_cast<const bf16x8*>(Ks + AT_KSWZ(32 + r32, cb));
;         p0 = __builtin_amdgcn_mfma_f32_32x32x16_bf16(b0, qr[d0], d0 == 0 ? negm : p0, 0, 0, 0);
;         p1 = __builtin_amdgcn_mfma_f32_32x32x16_bf16(b1, qr[d0], d0 == 0 ? negm : p1, 0, 0, 0); }
; }
.LBB4_870:
	v_exp_f32_e32 v182, v128
	v_exp_f32_e32 v230, v129
	v_exp_f32_e32 v231, v130
	v_exp_f32_e32 v232, v131
	v_exp_f32_e32 v233, v132
	v_exp_f32_e32 v234, v133
	v_exp_f32_e32 v235, v134
	v_exp_f32_e32 v236, v135
	v_exp_f32_e32 v237, v136
	v_exp_f32_e32 v238, v137
	v_exp_f32_e32 v239, v138
	v_exp_f32_e32 v240, v139
	v_exp_f32_e32 v241, v140
	v_exp_f32_e32 v242, v141
	v_exp_f32_e32 v243, v142
	v_exp_f32_e32 v244, v143
	v_add_u32_e32 v101, s76, v204
	v_add_u32_e32 v102, s76, v205
	v_add_u32_e32 v103, s76, v206
	ds_read_b128 v[172:175], v101 offset:49152
	ds_read_b128 v[176:179], v101 offset:53248
	ds_read_b128 v[214:217], v102 offset:49152
	ds_read_b128 v[218:221], v102 offset:53248
	ds_read_b128 v[222:225], v103 offset:49152
	ds_read_b128 v[226:229], v103 offset:53248
	v_exp_f32_e32 v112, v112
	v_exp_f32_e32 v113, v113
	v_exp_f32_e32 v114, v114
	s_waitcnt lgkmcnt(7)
	v_mfma_f32_32x32x16_bf16 v[128:143], v[96:99], v[156:159], v[80:95]
	s_add_u32 s34, s66, 0x2380c000
	s_addc_u32 s35, s67, 0
	s_add_u32 s66, s66, 0x2380e000
	s_addc_u32 s67, s67, 0
	s_add_u32 s74, s74, 0x21806000
	s_addc_u32 s75, s75, 0
	s_lshl_b32 s92, s63, 14
	s_add_i32 s92, s92, s94
	s_mov_b32 m0, s92
	s_lshl_b32 s96, s63, 13
	global_load_lds_dwordx4 v249, s[34:35]
	s_addk_i32 s92, 0x400
	s_mov_b32 m0, s92
	s_add_i32 s96, s96, s95
	global_load_lds_dwordx4 v250, s[34:35]
	s_nop 0
	s_mov_b32 m0, s96
	s_nop 0
	global_load_lds_dwordx4 v251, s[74:75]
	s_nop 0
	v_exp_f32_e32 v115, v115
	v_exp_f32_e32 v116, v116
	v_exp_f32_e32 v117, v117
	v_exp_f32_e32 v118, v118
	v_exp_f32_e32 v119, v119
	s_waitcnt lgkmcnt(6)
	v_mfma_f32_32x32x16_bf16 v[96:111], v[168:171], v[156:159], v[80:95]
	v_exp_f32_e32 v168, v120
	v_add_f32_e32 v120, 0, v182
	v_add_f32_e32 v120, v230, v120
	v_add_f32_e32 v120, v231, v120
	v_add_f32_e32 v120, v232, v120
	v_add_f32_e32 v120, v233, v120
	v_add_f32_e32 v120, v234, v120
	v_add_f32_e32 v120, v235, v120
	v_add_f32_e32 v120, v236, v120
	v_add_f32_e32 v120, v237, v120
	v_add_f32_e32 v120, v238, v120
	s_waitcnt lgkmcnt(5)
	v_mfma_f32_32x32x16_bf16 v[128:143], v[172:175], v[152:155], v[128:143]
	v_add_f32_e32 v120, v239, v120
	v_add_f32_e32 v120, v240, v120
	v_add_f32_e32 v120, v241, v120
	v_add_f32_e32 v120, v242, v120
	v_add_f32_e32 v120, v243, v120
	v_add_f32_e32 v120, v244, v120
	v_add_f32_e32 v120, v112, v120
	s_waitcnt lgkmcnt(4)
	v_mfma_f32_32x32x16_bf16 v[96:111], v[176:179], v[152:155], v[96:111]
	v_add_f32_e32 v120, v113, v120
	v_add_f32_e32 v120, v114, v120
	v_add_f32_e32 v120, v115, v120
	v_add_f32_e32 v120, v116, v120
	v_exp_f32_e32 v169, v121
	v_add_f32_e32 v120, v117, v120
	v_exp_f32_e32 v170, v122
	s_waitcnt lgkmcnt(3)
	v_mfma_f32_32x32x16_bf16 v[128:143], v[214:217], v[148:151], v[128:143]
	v_add_f32_e32 v120, v118, v120
	v_exp_f32_e32 v171, v123
	v_add_f32_e32 v120, v119, v120
	v_exp_f32_e32 v172, v124
	v_add_f32_e32 v120, v168, v120
	v_exp_f32_e32 v173, v125
	v_add_f32_e32 v120, v169, v120
	s_waitcnt lgkmcnt(2)
	v_mfma_f32_32x32x16_bf16 v[96:111], v[218:221], v[148:151], v[96:111]
	v_exp_f32_e32 v174, v126
	v_add_f32_e32 v120, v170, v120
	v_exp_f32_e32 v175, v127
	v_add_f32_e32 v120, v171, v120
	v_add_f32_e32 v120, v172, v120
	v_add_f32_e32 v120, v173, v120
	v_add_f32_e32 v120, v174, v120
	s_waitcnt lgkmcnt(1)
	v_mfma_f32_32x32x16_bf16 v[128:143], v[222:225], v[144:147], v[128:143]
	v_add_f32_e32 v213, v175, v120
	v_cvt_pk_bf16_f32 v120, v182, v230
	v_cvt_pk_bf16_f32 v121, v231, v232
	v_cvt_pk_bf16_f32 v122, v233, v234
	v_cvt_pk_bf16_f32 v123, v235, v236
	v_cvt_pk_bf16_f32 v124, v237, v238
	s_waitcnt lgkmcnt(0)
	v_mfma_f32_32x32x16_bf16 v[96:111], v[226:229], v[144:147], v[96:111]
	v_cvt_pk_bf16_f32 v125, v239, v240
	v_cvt_pk_bf16_f32 v126, v241, v242
	v_cvt_pk_bf16_f32 v127, v243, v244
	v_cvt_pk_bf16_f32 v112, v112, v113
	v_cvt_pk_bf16_f32 v113, v114, v115
	v_cvt_pk_bf16_f32 v114, v116, v117
	v_cvt_pk_bf16_f32 v115, v118, v119
	v_cvt_pk_bf16_f32 v116, v168, v169
	v_cvt_pk_bf16_f32 v117, v170, v171
	v_cvt_pk_bf16_f32 v118, v172, v173
	v_cvt_pk_bf16_f32 v119, v174, v175
	s_and_b64 vcc, exec, s[2:3]
	s_cbranch_vccnz .LBB4_872
	s_mov_b64 s[2:3], s[8:9]
	global_store_dwordx2 v188, v[184:185], s[2:3] nt

; DI void finishSM(f32x16& p0, f32x16& p1, float alpha, float& l_reg, bf16x8& pa0, bf16x8& pa1, bf16x8& pa2, bf16x8& pa3) {
; #pragma unroll
;     for (int r = 0; r < 16; ++r) p1[r] = __builtin_amdgcn_exp2f(p1[r]);
;     float ps = 0;
; #pragma unroll
;     for (int r = 0; r < 16; ++r) ps += p0[r];
; #pragma unroll
;     for (int r = 0; r < 16; ++r) ps += p1[r];
;     { auto rr = __builtin_amdgcn_permlane32_swap(__float_as_uint(ps), __float_as_uint(ps), false, false); ps = __uint_as_float(rr[0]) + __uint_as_float(rr[1]); }
;     l_reg = l_reg * alpha + ps;
;     ...
;     AT_PK4(p0, 0, pa0); AT_PK4(p0, 8, pa1); AT_PK4(p1, 0, pa2); AT_PK4(p1, 8, pa3);
;     ...
; }
; DI void qkt(f32x16& p0, f32x16& p1, const char* Ks, const bf16x8* qr, const f32x16& negm, int r32, int hi) {
; #pragma unroll
;     for (int d0 = 0; d0 < 4; ++d0) { const int cb = (d0 * 16 + hi * 8) * 2;
;         const bf16x8 b0 = *reinterpret_cast<const bf16x8*>(Ks + AT_KSWZ(r32, cb));
;         const bf16x8 b1 = *reinterpret_cast<const bf16x8*>(Ks + AT_KSWZ(32 + r32, cb));
;         p0 = __builtin_amdgcn_mfma_f32_32x32x16_bf16(b0, qr[d0], d0 == 0 ? negm : p0, 0, 0, 0);
;         p1 = __builtin_amdgcn_mfma_f32_32x32x16_bf16(b1, qr[d0], d0 == 0 ? negm : p1, 0, 0, 0); }
; }
.LBB4_923:
	s_lshl_b32 s18, s30, 13
	s_add_i32 s18, s18, 0
	v_add_u32_e32 v72, s18, v208
	v_add_u32_e32 v112, s18, v209
	v_add_u32_e32 v180, s18, v210
	s_waitcnt lgkmcnt(1)
	v_mfma_f32_32x32x16_bf16 v[128:143], v[64:67], v[156:159], v[80:95]
	ds_read_b128 v[64:67], v72 offset:49152
	ds_read_b128 v[72:75], v72 offset:53248
	ds_read_b128 v[76:79], v112 offset:49152
	ds_read_b128 v[224:227], v112 offset:53248
	s_add_u32 s34, s46, s16
	s_addc_u32 s35, s47, s17
	s_add_u32 s24, s34, 0x23808000
	s_addc_u32 s25, s35, 0
	s_add_u32 s54, s34, 0x2380a000
	s_add_u32 s42, s46, s20
	s_addc_u32 s43, s47, s21
	s_add_u32 s56, s42, 0x21884000
	s_addc_u32 s57, s43, 0
	s_lshl_b32 s92, s15, 14
	s_add_i32 s92, s92, s94
	s_mov_b32 m0, s92
	s_lshl_b32 s96, s15, 13
	global_load_lds_dwordx4 v249, s[24:25]
	s_addk_i32 s92, 0x400
	s_mov_b32 m0, s92
	s_add_i32 s96, s96, s95
	global_load_lds_dwordx4 v250, s[24:25]
	s_nop 0
	s_mov_b32 m0, s96
	s_nop 0
	global_load_lds_dwordx4 v251, s[56:57]
	v_exp_f32_e32 v182, v97
	v_exp_f32_e32 v217, v98
	v_exp_f32_e32 v218, v99
	v_exp_f32_e32 v223, v100
	v_exp_f32_e32 v232, v101
	s_waitcnt lgkmcnt(4)
	v_mfma_f32_32x32x16_bf16 v[112:127], v[68:71], v[156:159], v[80:95]
	ds_read_b128 v[68:71], v180 offset:49152
	ds_read_b128 v[228:231], v180 offset:53248
	v_exp_f32_e32 v180, v96
	v_cvt_pk_bf16_f32 v96, v220, v222
	v_cvt_pk_bf16_f32 v97, v179, v221
	v_cvt_pk_bf16_f32 v98, v177, v219
	v_cvt_pk_bf16_f32 v99, v176, v178
	s_waitcnt lgkmcnt(4)
	v_mfma_f32_32x32x16_bf16 v[112:127], v[72:75], v[152:155], v[112:127]
	v_add_f32_e32 v75, 0, v220
	v_add_f32_e32 v75, v222, v75
	v_add_f32_e32 v75, v179, v75
	v_add_f32_e32 v75, v221, v75
	v_add_f32_e32 v75, v177, v75
	v_add_f32_e32 v75, v219, v75
	v_add_f32_e32 v75, v176, v75
	v_mfma_f32_32x32x16_bf16 v[128:143], v[64:67], v[152:155], v[128:143]
	v_add_f32_e32 v75, v178, v75
	v_add_f32_e32 v75, v173, v75
	v_add_f32_e32 v75, v175, v75
	v_add_f32_e32 v75, v171, v75
	v_add_f32_e32 v75, v174, v75
	v_add_f32_e32 v75, v169, v75
	v_add_f32_e32 v75, v172, v75
	s_waitcnt lgkmcnt(3)
	v_mfma_f32_32x32x16_bf16 v[128:143], v[76:79], v[148:151], v[128:143]
	v_add_f32_e32 v75, v168, v75
	v_add_f32_e32 v75, v170, v75
	v_add_f32_e32 v75, v180, v75
	v_add_f32_e32 v75, v182, v75
	v_exp_f32_e32 v64, v102
	v_exp_f32_e32 v65, v103
	v_exp_f32_e32 v66, v104
	s_waitcnt lgkmcnt(2)
	v_mfma_f32_32x32x16_bf16 v[112:127], v[224:227], v[148:151], v[112:127]
	v_exp_f32_e32 v67, v105
	v_exp_f32_e32 v105, v106
	v_exp_f32_e32 v106, v107
	v_exp_f32_e32 v107, v108
	v_exp_f32_e32 v72, v109
	v_exp_f32_e32 v73, v110
	v_exp_f32_e32 v74, v111
	s_waitcnt lgkmcnt(1)
	v_mfma_f32_32x32x16_bf16 v[128:143], v[68:71], v[144:147], v[128:143]
	v_add_f32_e32 v68, v217, v75
	v_add_f32_e32 v68, v218, v68
	v_add_f32_e32 v68, v223, v68
	v_add_f32_e32 v68, v232, v68
	v_add_f32_e32 v68, v64, v68
	v_add_f32_e32 v68, v65, v68
	v_add_f32_e32 v68, v66, v68
	v_add_f32_e32 v68, v67, v68
	s_waitcnt lgkmcnt(0)
	v_mfma_f32_32x32x16_bf16 v[112:127], v[228:231], v[144:147], v[112:127]
	v_add_f32_e32 v68, v105, v68
	v_add_f32_e32 v68, v106, v68
	v_add_f32_e32 v68, v107, v68
	v_add_f32_e32 v68, v72, v68
	v_add_f32_e32 v68, v73, v68
	v_add_f32_e32 v215, v74, v68
	v_cvt_pk_bf16_f32 v108, v173, v175
	v_cvt_pk_bf16_f32 v109, v171, v174
	v_cvt_pk_bf16_f32 v110, v169, v172
	v_cvt_pk_bf16_f32 v111, v168, v170
	v_cvt_pk_bf16_f32 v100, v180, v182
	v_cvt_pk_bf16_f32 v101, v217, v218
	v_cvt_pk_bf16_f32 v102, v223, v232
	v_cvt_pk_bf16_f32 v103, v64, v65
	v_cvt_pk_bf16_f32 v104, v66, v67
	v_cvt_pk_bf16_f32 v105, v105, v106
	v_cvt_pk_bf16_f32 v106, v107, v72
	v_cvt_pk_bf16_f32 v107, v73, v74
	s_addc_u32 s55, s35, 0
	s_andn2_b64 vcc, exec, s[2:3]
	s_cbranch_vccnz .LBB4_925
	s_mov_b64 s[2:3], s[8:9]
	global_store_dwordx2 v193, v[184:185], s[2:3] nt

; DI void finishSM(f32x16& p0, f32x16& p1, float alpha, float& l_reg, bf16x8& pa0, bf16x8& pa1, bf16x8& pa2, bf16x8& pa3) {
; #pragma unroll
;     for (int r = 0; r < 16; ++r) p1[r] = __builtin_amdgcn_exp2f(p1[r]);
;     float ps = 0;
; #pragma unroll
;     for (int r = 0; r < 16; ++r) ps += p0[r];
; #pragma unroll
;     for (int r = 0; r < 16; ++r) ps += p1[r];
;     { auto rr = __builtin_amdgcn_permlane32_swap(__float_as_uint(ps), __float_as_uint(ps), false, false); ps = __uint_as_float(rr[0]) + __uint_as_float(rr[1]); }
;     l_reg = l_reg * alpha + ps;
;     ...
;     AT_PK4(p0, 0, pa0); AT_PK4(p0, 8, pa1); AT_PK4(p1, 0, pa2); AT_PK4(p1, 8, pa3);
;     ...
; }
; DI void qkt(f32x16& p0, f32x16& p1, const char* Ks, const bf16x8* qr, const f32x16& negm, int r32, int hi) {
; #pragma unroll
;     for (int d0 = 0; d0 < 4; ++d0) { const int cb = (d0 * 16 + hi * 8) * 2;
;         const bf16x8 b0 = *reinterpret_cast<const bf16x8*>(Ks + AT_KSWZ(r32, cb));
;         const bf16x8 b1 = *reinterpret_cast<const bf16x8*>(Ks + AT_KSWZ(32 + r32, cb));
;         p0 = __builtin_amdgcn_mfma_f32_32x32x16_bf16(b0, qr[d0], d0 == 0 ? negm : p0, 0, 0, 0);
;         p1 = __builtin_amdgcn_mfma_f32_32x32x16_bf16(b1, qr[d0], d0 == 0 ? negm : p1, 0, 0, 0); }
; }
.LBB4_944:
	v_exp_f32_e32 v182, v128
	v_exp_f32_e32 v234, v129
	v_exp_f32_e32 v235, v130
	v_exp_f32_e32 v236, v131
	v_exp_f32_e32 v237, v132
	v_exp_f32_e32 v238, v133
	v_exp_f32_e32 v239, v134
	v_exp_f32_e32 v240, v135
	v_exp_f32_e32 v241, v136
	v_exp_f32_e32 v242, v137
	v_exp_f32_e32 v243, v138
	v_exp_f32_e32 v244, v139
	v_exp_f32_e32 v245, v140
	v_exp_f32_e32 v246, v141
	v_exp_f32_e32 v247, v142
	v_exp_f32_e32 v248, v143
	v_add_u32_e32 v101, s54, v208
	v_add_u32_e32 v102, s54, v209
	v_add_u32_e32 v103, s54, v210
	ds_read_b128 v[172:175], v101 offset:49152
	ds_read_b128 v[176:179], v101 offset:53248
	ds_read_b128 v[218:221], v102 offset:49152
	ds_read_b128 v[222:225], v102 offset:53248
	ds_read_b128 v[226:229], v103 offset:49152
	ds_read_b128 v[230:233], v103 offset:53248
	v_exp_f32_e32 v112, v112
	v_exp_f32_e32 v113, v113
	v_exp_f32_e32 v114, v114
	s_waitcnt lgkmcnt(7)
	v_mfma_f32_32x32x16_bf16 v[128:143], v[96:99], v[156:159], v[80:95]
	s_add_u32 s24, s34, 0x2380c000
	s_addc_u32 s25, s35, 0
	s_add_u32 s34, s34, 0x2380e000
	s_addc_u32 s35, s35, 0
	s_add_u32 s42, s42, 0x21886000
	s_addc_u32 s43, s43, 0
	s_lshl_b32 s92, s29, 14
	s_add_i32 s92, s92, s94
	s_mov_b32 m0, s92
	s_lshl_b32 s96, s29, 13
	global_load_lds_dwordx4 v249, s[24:25]
	s_addk_i32 s92, 0x400
	s_mov_b32 m0, s92
	s_add_i32 s96, s96, s95
	global_load_lds_dwordx4 v250, s[24:25]
	s_nop 0
	s_mov_b32 m0, s96
	s_nop 0
	global_load_lds_dwordx4 v251, s[42:43]
	s_nop 0
	v_exp_f32_e32 v115, v115
	v_exp_f32_e32 v116, v116
	v_exp_f32_e32 v117, v117
	v_exp_f32_e32 v118, v118
	v_exp_f32_e32 v119, v119
	s_waitcnt lgkmcnt(6)
	v_mfma_f32_32x32x16_bf16 v[96:111], v[168:171], v[156:159], v[80:95]
	v_exp_f32_e32 v168, v120
	v_add_f32_e32 v120, 0, v182
	v_add_f32_e32 v120, v234, v120
	v_add_f32_e32 v120, v235, v120
	v_add_f32_e32 v120, v236, v120
	v_add_f32_e32 v120, v237, v120
	v_add_f32_e32 v120, v238, v120
	v_add_f32_e32 v120, v239, v120
	v_add_f32_e32 v120, v240, v120
	v_add_f32_e32 v120, v241, v120
	v_add_f32_e32 v120, v242, v120
	s_waitcnt lgkmcnt(5)
	v_mfma_f32_32x32x16_bf16 v[128:143], v[172:175], v[152:155], v[128:143]
	v_add_f32_e32 v120, v243, v120
	v_add_f32_e32 v120, v244, v120
	v_add_f32_e32 v120, v245, v120
	v_add_f32_e32 v120, v246, v120
	v_add_f32_e32 v120, v247, v120
	v_add_f32_e32 v120, v248, v120
	v_add_f32_e32 v120, v112, v120
	s_waitcnt lgkmcnt(4)
	v_mfma_f32_32x32x16_bf16 v[96:111], v[176:179], v[152:155], v[96:111]
	v_add_f32_e32 v120, v113, v120
	v_add_f32_e32 v120, v114, v120
	v_add_f32_e32 v120, v115, v120
	v_add_f32_e32 v120, v116, v120
	v_exp_f32_e32 v169, v121
	v_add_f32_e32 v120, v117, v120
	v_exp_f32_e32 v170, v122
	s_waitcnt lgkmcnt(3)
	v_mfma_f32_32x32x16_bf16 v[128:143], v[218:221], v[148:151], v[128:143]
	v_add_f32_e32 v120, v118, v120
	v_exp_f32_e32 v171, v123
	v_add_f32_e32 v120, v119, v120
	v_exp_f32_e32 v172, v124
	v_add_f32_e32 v120, v168, v120
	v_exp_f32_e32 v173, v125
	v_add_f32_e32 v120, v169, v120
	s_waitcnt lgkmcnt(2)
	v_mfma_f32_32x32x16_bf16 v[96:111], v[222:225], v[148:151], v[96:111]
	v_exp_f32_e32 v174, v126
	v_add_f32_e32 v120, v170, v120
	v_exp_f32_e32 v175, v127
	v_add_f32_e32 v120, v171, v120
	v_add_f32_e32 v120, v172, v120
	v_add_f32_e32 v120, v173, v120
	v_add_f32_e32 v120, v174, v120
	s_waitcnt lgkmcnt(1)
	v_mfma_f32_32x32x16_bf16 v[128:143], v[226:229], v[144:147], v[128:143]
	v_add_f32_e32 v217, v175, v120
	v_cvt_pk_bf16_f32 v120, v182, v234
	v_cvt_pk_bf16_f32 v121, v235, v236
	v_cvt_pk_bf16_f32 v122, v237, v238
	v_cvt_pk_bf16_f32 v123, v239, v240
	v_cvt_pk_bf16_f32 v124, v241, v242
	s_waitcnt lgkmcnt(0)
	v_mfma_f32_32x32x16_bf16 v[96:111], v[230:233], v[144:147], v[96:111]
	v_cvt_pk_bf16_f32 v125, v243, v244
	v_cvt_pk_bf16_f32 v126, v245, v246
	v_cvt_pk_bf16_f32 v127, v247, v248
	v_cvt_pk_bf16_f32 v112, v112, v113
	v_cvt_pk_bf16_f32 v113, v114, v115
	v_cvt_pk_bf16_f32 v114, v116, v117
	v_cvt_pk_bf16_f32 v115, v118, v119
	v_cvt_pk_bf16_f32 v116, v168, v169
	v_cvt_pk_bf16_f32 v117, v170, v171
	v_cvt_pk_bf16_f32 v118, v172, v173
	v_cvt_pk_bf16_f32 v119, v174, v175
	s_and_b64 vcc, exec, s[2:3]
	s_cbranch_vccnz .LBB4_946
	s_mov_b64 s[2:3], s[8:9]
	global_store_dwordx2 v193, v[184:185], s[2:3] nt
